# speedup vs baseline: 1.0136x; 1.0056x over previous
.LBB0_71:
	s_or_b64 exec, exec, s[4:5]
	v_cmp_lt_i32_e64 s[8:9], -1, v11
	v_lshlrev_b32_e32 v11, 2, v11
	s_and_saveexec_b64 s[4:5], s[8:9]
	v_mov_b32_e32 v7, 1
	ds_add_rtn_u32 v7, v11, v7 offset:16384
	s_or_b64 exec, exec, s[4:5]
	v_cmp_lt_i32_e64 s[4:5], -1, v12
	v_lshlrev_b32_e32 v12, 2, v12
	s_and_saveexec_b64 s[6:7], s[4:5]
	v_mov_b32_e32 v8, 1
	ds_add_rtn_u32 v8, v12, v8 offset:16384
	s_or_b64 exec, exec, s[6:7]
	v_or_b32_e32 v14, 0x4000, v1
	v_cmp_lt_i32_e64 s[6:7], -1, v13
	v_lshlrev_b32_e32 v13, 2, v13
	s_and_saveexec_b64 s[10:11], s[6:7]
	v_mov_b32_e32 v9, 1
	ds_add_rtn_u32 v9, v13, v9 offset:16384
	s_or_b64 exec, exec, s[10:11]
	s_waitcnt lgkmcnt(0)
	s_barrier
	ds_read_b32 v15, v14
	v_and_b32_e32 v18, 63, v0
	v_mov_b32_e32 v17, 0
	v_cmp_eq_u32_e64 s[10:11], 63, v18
	v_lshrrev_b32_e32 v19, 6, v0
	s_waitcnt lgkmcnt(0)
	v_add_u32_dpp v16, v15, v15 row_shr:1 row_mask:0xf bank_mask:0xf bound_ctrl:1
	s_nop 1
	v_add_u32_dpp v16, v16, v16 row_shr:2 row_mask:0xf bank_mask:0xf bound_ctrl:1
	s_nop 1
	v_add_u32_dpp v16, v16, v16 row_shr:4 row_mask:0xf bank_mask:0xf bound_ctrl:1
	s_nop 1
	v_add_u32_dpp v16, v16, v16 row_shr:8 row_mask:0xf bank_mask:0xf bound_ctrl:1
	s_nop 1
	v_add_u32_dpp v16, v16, v16 row_bcast:15 row_mask:0xa bank_mask:0xf
	s_nop 1
	v_add_u32_dpp v16, v16, v16 row_bcast:31 row_mask:0xc bank_mask:0xf
	s_and_saveexec_b64 s[12:13], s[10:11]
	v_lshlrev_b32_e32 v18, 2, v19
	ds_write_b32 v18, v16 offset:20480
	s_or_b64 exec, exec, s[12:13]
	s_load_dwordx4 s[12:15], s[0:1], 0x30
	v_cmp_lt_u32_e64 s[0:1], 63, v0
	s_waitcnt lgkmcnt(0)
	s_barrier
	v_readfirstlane_b32 s16, v19
	v_and_b32_e32 v18, 63, v0
	v_min_u32_e32 v20, 15, v18
	v_lshlrev_b32_e32 v20, 2, v20
	ds_read_b32 v17, v20 offset:20480
	v_cmp_gt_u32_e64 s[18:19], s16, v18
	s_waitcnt lgkmcnt(0)
	s_nop 1
	v_cndmask_b32_e64 v17, 0, v17, s[18:19]
	s_nop 1
	v_add_u32_dpp v17, v17, v17 row_shr:1 row_mask:0xf bank_mask:0xf bound_ctrl:1
	s_nop 1
	v_add_u32_dpp v17, v17, v17 row_shr:2 row_mask:0xf bank_mask:0xf bound_ctrl:1
	s_nop 1
	v_add_u32_dpp v17, v17, v17 row_shr:4 row_mask:0xf bank_mask:0xf bound_ctrl:1
	s_nop 1
	v_add_u32_dpp v17, v17, v17 row_shr:8 row_mask:0xf bank_mask:0xf bound_ctrl:1
	s_nop 1
	v_readlane_b32 s17, v17, 15
	s_nop 3
	v_mov_b32_e32 v17, s17
	v_sub_u32_e32 v15, v16, v15
	s_movk_i32 s0, 0x3fe
	v_add_u32_e32 v15, v15, v17
	v_cmp_gt_u32_e64 s[0:1], s0, v0
	ds_write_b32 v14, v15
	s_waitcnt lgkmcnt(0)
	s_barrier
	s_and_saveexec_b64 s[10:11], s[0:1]
	s_cbranch_execz .LBB0_99
	ds_read_b32 v16, v14
	s_mulk_i32 s2, 0x3fe
	v_add_u32_e32 v14, s2, v0
	v_ashrrev_i32_e32 v15, 31, v14
	v_lshl_add_u64 v[14:15], v[14:15], 2, s[14:15]
	s_waitcnt lgkmcnt(0)
	global_store_dword v[14:15], v16, off sc1
	s_or_b64 exec, exec, s[10:11]
	s_and_saveexec_b64 s[0:1], vcc
	s_cbranch_execnz .LBB0_100
